# v77 + P6 item prologue de-serialised: 17 router/row loads issued first, gamma staging loads join them, one vmcnt(0) instead of three
# speedup vs baseline: 1.0047x; 1.0047x over previous
; #define LAS __attribute__((address_space(3)))
; template <bool DRY> __device__ __forceinline__ void p6_item(Ctx& F, int item) {
;     ...
;     for (int i = tid; i < DM / 4; i += NWAVES * 64) { *(LAS f32x4*)(ggL + 4 * i) = *(const f32x4*)((const float*)F.in[17] + 4 * i) * (*(const f32x4*)(mod + 4 * DM + 4 * i) + 1.0f); *(LAS f32x4*)(shL + 4 * i) = *(const f32x4*)(mod + 3 * DM + 4 * i); }
;     const float brl = ((const float*)F.in[19])[lane]; const int g = lane >> 3;
;     unsigned lc = 0u;
;     bf16x8 bw[2][4];
; #pragma unroll
;     for (int ks = 0; ks < 2; ++ks)
; #pragma unroll
;         for (int et = 0; et < 4; ++et) bw[ks][et] = *(const bf16x8*)(Wr + (size_t)(16 * et + fr) * DM + 256 * w + 32 * ks + 8 * fq);
;     u32x4 xq[2][4];
; #pragma unroll
;     for (int i = 0; i < 2; ++i)
; #pragma unroll
;         for (int j = 0; j < 4; ++j) xq[i][j] = *(const u32x4*)(x1 + (size_t)(t0 + 2 * w + i) * DM + 8 * lane + 512 * j);
;     __syncthreads();
;     bf16x8 bw2[6][4];
; #pragma unroll
;     for (int ks = 0; ks < 3; ++ks)
; #pragma unroll
;         for (int et = 0; et < 4; ++et) bw2[ks][et] = *(const bf16x8*)(Wr + (size_t)(16 * et + fr) * DM + 256 * w + 64 + 32 * ks + 8 * fq);
.LBB0_581:
	v_readlane_b32 s0, v255, 3
	s_lshl_b32 s1, s0, 6
	v_readlane_b32 s0, v254, 59
	s_add_i32 s0, s1, s0
	v_writelane_b32 v255, s1, 16
	s_ashr_i32 s1, s0, 31
	s_lshl_b64 s[22:23], s[0:1], 12
	s_or_b32 s0, s0, 1
	s_ashr_i32 s1, s0, 31
	s_lshl_b64 s[0:1], s[0:1], 12
	s_waitcnt vmcnt(0)
	v_lshl_add_u64 v[46:47], v[134:135], 0, s[22:23]
	v_lshl_add_u64 v[50:51], v[134:135], 0, s[0:1]
	global_load_dword v153, v[118:119], off
	global_load_dwordx4 v[2:5], v[122:123], off
	global_load_dwordx4 v[6:9], v[124:125], off
	global_load_dwordx4 v[10:13], v[120:121], off
	global_load_dwordx4 v[14:17], v[120:121], off offset:64
	global_load_dwordx4 v[18:21], v[126:127], off
	global_load_dwordx4 v[22:25], v[128:129], off
	global_load_dwordx4 v[26:29], v[130:131], off
	global_load_dwordx4 v[30:33], v[132:133], off
	global_load_dwordx4 v[34:37], v[46:47], off
	global_load_dwordx4 v[38:41], v[46:47], off offset:1024
	global_load_dwordx4 v[42:45], v[46:47], off offset:2048
	s_nop 0
	global_load_dwordx4 v[46:49], v[46:47], off offset:3072
	s_nop 0
	global_load_dwordx4 v[78:81], v[50:51], off
	global_load_dwordx4 v[90:93], v[50:51], off offset:1024
	global_load_dwordx4 v[102:105], v[50:51], off offset:2048
	global_load_dwordx4 v[110:113], v[50:51], off offset:3072
	s_mov_b64 s[0:1], exec
	v_readlane_b32 s22, v254, 10
	v_readlane_b32 s23, v254, 11
	s_and_b64 s[22:23], s[0:1], s[22:23]
	s_mov_b64 exec, s[22:23]
	s_cbranch_execz .LBB0_583
	v_readlane_b32 s5, v255, 3
	s_ashr_i32 s3, s5, 31
	s_lshr_b32 s3, s3, 27
	s_add_i32 s3, s5, s3
	s_ashr_i32 s3, s3, 5
	s_mul_i32 s22, s3, 6
	s_ashr_i32 s23, s22, 31
	s_lshl_b64 s[22:23], s[22:23], 13
	v_readlane_b32 s3, v254, 12
	s_add_u32 s22, s3, s22
	v_readlane_b32 s3, v254, 13
	s_addc_u32 s23, s3, s23
	v_mov_b32_e32 v170, v152
	v_mov_b32_e32 v171, v115
	v_lshl_add_u64 v[162:163], s[22:23], 0, v[170:171]
	s_mov_b32 s3, 0x8000
	v_add_co_u32_e32 v158, vcc, s3, v162
	global_load_dwordx4 v[154:157], v[116:117], off
	s_nop 0
	v_addc_co_u32_e32 v159, vcc, 0, v163, vcc
	global_load_dwordx4 v[158:161], v[158:159], off
	v_add_co_u32_e32 v164, vcc, 0x6000, v162
	s_nop 1
	v_addc_co_u32_e32 v165, vcc, 0, v163, vcc
	global_load_dwordx4 v[164:167], v[164:165], off
	s_waitcnt vmcnt(0)
	v_pk_add_f32 v[160:161], v[160:161], 1.0 op_sel_hi:[1,0]
	v_pk_add_f32 v[158:159], v[158:159], 1.0 op_sel_hi:[1,0]
	v_pk_mul_f32 v[156:157], v[156:157], v[160:161]
	v_pk_mul_f32 v[154:155], v[154:155], v[158:159]
	ds_write_b128 v217, v[154:157]
	ds_write_b128 v231, v[164:167]
.LBB0_583:
	s_or_b64 exec, exec, s[0:1]
	s_waitcnt vmcnt(0) lgkmcnt(0)
	s_barrier
	global_load_dwordx4 v[50:53], v[136:137], off offset:128
	global_load_dwordx4 v[54:57], v[136:137], off offset:192
	global_load_dwordx4 v[58:61], v[140:141], off offset:128
	global_load_dwordx4 v[62:65], v[140:141], off offset:192
	global_load_dwordx4 v[66:69], v[138:139], off offset:128
	global_load_dwordx4 v[70:73], v[136:137], off offset:256
	global_load_dwordx4 v[74:77], v[138:139], off offset:192
	global_load_dwordx4 v[82:85], v[138:139], off offset:256
	global_load_dwordx4 v[86:89], v[142:143], off offset:128
	global_load_dwordx4 v[94:97], v[140:141], off offset:256
	global_load_dwordx4 v[98:101], v[142:143], off offset:192
	global_load_dwordx4 v[106:109], v[142:143], off offset:256
	v_readlane_b32 s0, v254, 62
	s_mov_b32 s74, 0
	v_mov_b32_e32 v216, 0
	s_mov_b32 s66, s0
	s_branch .LBB0_585
